# depthwise-weight copy: counted vmcnt waits at each ds_write (first consumer) instead of one vmcnt(0) before all 31 LDS writes
# speedup vs baseline: 1.0036x; 1.0036x over previous
; #define LAS __attribute__((address_space(3)))
; #define INL(off) (INR(pb + (off)) && !((PH_DIS >> (1 + (off))) & 1) && (!probe_ || ((PROBE_COLD >> (off)) & 1)))
; #define LAUNDER MKCTX; asm volatile("" : "+v"(C.tid), "+v"(C.lane), "+v"(C.gtid)); asm volatile("" : "+s"(C.blk), "+s"(C.vcu), "+s"(C.gw)); PTRS
; __device__ __forceinline__ void convpre_phase(const Ctx& C, const bf16* Z, const float* dw_w, const float* dw_b, const float* ln_g, const float* ln_b, bf16* ZC) {
;     const __amdgpu_buffer_rsrc_t zrs = __builtin_amdgcn_make_buffer_rsrc((void*)ZC, (short)0, T * CONV_CH * 2, 0x00020000);
;     LAS float* wl = (LAS float*)(C.lds + RING_OFF);
;     LAS bf16* zs = (LAS bf16*)(C.lds + RING_OFF + 63488);
;     __syncthreads();
;     for (int i = C.tid; i < CONV_W * CONV_CH; i += 512) wl[i] = dw_w[i];
; __global__ void __launch_bounds__(512, 2) mega_fwd(Args args) {
;     ...
;         if (INL(2)) for (int rep_ = 0; rep_ < NREP(3); ++rep_) { LAUNDER;
;             unsigned* zc_cnt = (unsigned*)(ws + WS_CTL) + CW_ZC + 64 * l + 2048 * rep_ + (probe_ ? 4096 : 0);
;             convpre_phase(C, Zb, GIN(4) + l * CONV_W * CONV_CH, GIN(5) + l * CONV_CH, GIN(6) + l * CONV_CH, GIN(7) + l * CONV_CH, ZC);
.LBB0_461:
	v_readlane_b32 s0, v254, 20
	s_mul_i32 s0, s0, 10
	v_readlane_b32 s8, v253, 8
	s_add_i32 s2, s0, 3
	v_readlane_b32 s12, v253, 12
	v_readlane_b32 s1, v254, 21
	v_readlane_b32 s13, v253, 13
	s_cmp_le_i32 s12, s2
	s_cselect_b64 s[0:1], -1, 0
	s_cmp_lt_i32 s2, s13
	s_cselect_b64 s[2:3], -1, 0
	s_and_b64 s[0:1], s[0:1], s[2:3]
	v_writelane_b32 v254, s0, 23
	v_readlane_b32 s10, v253, 10
	v_readlane_b32 s11, v253, 11
	v_writelane_b32 v254, s1, 24
	s_andn2_b64 vcc, exec, s[0:1]
	v_readlane_b32 s9, v253, 9
	v_readlane_b32 s14, v253, 14
	v_readlane_b32 s15, v253, 15
	s_cbranch_vccnz .LBB0_665
	v_readlane_b32 s0, v253, 16
	v_mbcnt_lo_u32_b32 v218, -1, 0
	v_mbcnt_hi_u32_b32 v218, -1, v218
	v_readlane_b32 s2, v253, 17
	s_mov_b64 s[4:5], s[10:11]
	v_add_u32_e32 v202, s0, v218
	v_readlane_b32 s0, v253, 19
	v_readlane_b32 s12, v253, 1
	v_readlane_b32 s13, v253, 2
	v_add_u32_e32 v219, s0, v202
	v_readlane_b32 s0, v253, 0
	s_mov_b32 s1, s0
	v_readlane_b32 s0, v253, 18
	s_nop 0
	v_writelane_b32 v254, s2, 25
	v_writelane_b32 v254, s1, 26
	s_nop 0
	v_readlane_b32 s0, v254, 3
	v_readlane_b32 s1, v254, 4
	v_readlane_b32 s2, v254, 5
	v_readlane_b32 s3, v254, 6
	s_add_u32 s0, s4, 0x41000000
	v_writelane_b32 v254, s0, 3
	s_nop 1
	v_writelane_b32 v254, s1, 4
	v_writelane_b32 v254, s2, 5
	v_writelane_b32 v254, s3, 6
	v_writelane_b32 v254, s4, 27
	s_addc_u32 s0, s5, 0
	s_nop 0
	v_writelane_b32 v254, s5, 28
	v_writelane_b32 v254, s0, 29
	v_writelane_b32 v254, s12, 30
	s_load_dwordx8 s[4:11], s[12:13], 0x20
	s_movk_i32 s0, 0x3e00
	v_writelane_b32 v254, s13, 31
	v_cmp_gt_i32_e32 vcc, s0, v202
	s_waitcnt vmcnt(0) lgkmcnt(0)
	s_barrier
	s_and_saveexec_b64 s[0:1], vcc
	s_cbranch_execz .LBB0_475
	v_readlane_b32 s12, v254, 20
	v_lshlrev_b32_e32 v0, 2, v202
	s_mul_i32 s30, s12, 0x3e00
	s_lshl_b64 s[12:13], s[30:31], 2
	s_add_u32 s12, s4, s12
	s_addc_u32 s13, s5, s13
	global_load_dword v4, v0, s[12:13]
	global_load_dword v5, v0, s[12:13] offset:2048
	s_add_u32 s12, s12, 0x1000
	s_addc_u32 s13, s13, 0
	global_load_dword v6, v0, s[12:13]
	global_load_dword v7, v0, s[12:13] offset:2048
	s_add_u32 s12, s12, 0x1000
	s_addc_u32 s13, s13, 0
	global_load_dword v8, v0, s[12:13]
	global_load_dword v9, v0, s[12:13] offset:2048
	s_add_u32 s12, s12, 0x1000
	s_addc_u32 s13, s13, 0
	global_load_dword v10, v0, s[12:13]
	global_load_dword v11, v0, s[12:13] offset:2048
	s_add_u32 s12, s12, 0x1000
	s_addc_u32 s13, s13, 0
	global_load_dword v12, v0, s[12:13]
	global_load_dword v13, v0, s[12:13] offset:2048
	s_add_u32 s12, s12, 0x1000
	s_addc_u32 s13, s13, 0
	global_load_dword v14, v0, s[12:13]
	global_load_dword v15, v0, s[12:13] offset:2048
	s_add_u32 s12, s12, 0x1000
	s_addc_u32 s13, s13, 0
	global_load_dword v16, v0, s[12:13]
	global_load_dword v17, v0, s[12:13] offset:2048
	s_add_u32 s12, s12, 0x1000
	s_addc_u32 s13, s13, 0
	global_load_dword v18, v0, s[12:13]
	global_load_dword v19, v0, s[12:13] offset:2048
	s_add_u32 s12, s12, 0x1000
	s_addc_u32 s13, s13, 0
	global_load_dword v20, v0, s[12:13]
	global_load_dword v21, v0, s[12:13] offset:2048
	s_add_u32 s12, s12, 0x1000
	s_addc_u32 s13, s13, 0
	global_load_dword v22, v0, s[12:13]
	global_load_dword v23, v0, s[12:13] offset:2048
	s_add_u32 s12, s12, 0x1000
	s_addc_u32 s13, s13, 0
	global_load_dword v24, v0, s[12:13]
	global_load_dword v25, v0, s[12:13] offset:2048
	s_add_u32 s12, s12, 0x1000
	s_addc_u32 s13, s13, 0
	global_load_dword v26, v0, s[12:13]
	global_load_dword v27, v0, s[12:13] offset:2048
	s_add_u32 s12, s12, 0x1000
	s_addc_u32 s13, s13, 0
	global_load_dword v28, v0, s[12:13]
	global_load_dword v29, v0, s[12:13] offset:2048
	s_add_u32 s12, s12, 0x1000
	s_addc_u32 s13, s13, 0
	global_load_dword v30, v0, s[12:13]
	global_load_dword v31, v0, s[12:13] offset:2048
	s_add_u32 s12, s12, 0x1000
	s_addc_u32 s13, s13, 0
	global_load_dword v32, v0, s[12:13]
	global_load_dword v33, v0, s[12:13] offset:2048
	s_add_u32 s12, s12, 0x1000
	s_addc_u32 s13, s13, 0
	global_load_dword v34, v0, s[12:13]
	s_waitcnt vmcnt(30)
	ds_write_b32 v0, v4
	s_waitcnt vmcnt(29)
	ds_write_b32 v0, v5 offset:2048
	s_waitcnt vmcnt(28)
	ds_write_b32 v0, v6 offset:4096
	s_waitcnt vmcnt(27)
	ds_write_b32 v0, v7 offset:6144
	s_waitcnt vmcnt(26)
	ds_write_b32 v0, v8 offset:8192
	s_waitcnt vmcnt(25)
	ds_write_b32 v0, v9 offset:10240
	s_waitcnt vmcnt(24)
	ds_write_b32 v0, v10 offset:12288
	s_waitcnt vmcnt(23)
	ds_write_b32 v0, v11 offset:14336
	s_waitcnt vmcnt(22)
	ds_write_b32 v0, v12 offset:16384
	s_waitcnt vmcnt(21)
	ds_write_b32 v0, v13 offset:18432
	s_waitcnt vmcnt(20)
	ds_write_b32 v0, v14 offset:20480
	s_waitcnt vmcnt(19)
	ds_write_b32 v0, v15 offset:22528
	s_waitcnt vmcnt(18)
	ds_write_b32 v0, v16 offset:24576
	s_waitcnt vmcnt(17)
	ds_write_b32 v0, v17 offset:26624
	s_waitcnt vmcnt(16)
	ds_write_b32 v0, v18 offset:28672
	s_waitcnt vmcnt(15)
	ds_write_b32 v0, v19 offset:30720
	s_waitcnt vmcnt(14)
	ds_write_b32 v0, v20 offset:32768
	s_waitcnt vmcnt(13)
	ds_write_b32 v0, v21 offset:34816
	s_waitcnt vmcnt(12)
	ds_write_b32 v0, v22 offset:36864
	s_waitcnt vmcnt(11)
	ds_write_b32 v0, v23 offset:38912
	s_waitcnt vmcnt(10)
	ds_write_b32 v0, v24 offset:40960
	s_waitcnt vmcnt(9)
	ds_write_b32 v0, v25 offset:43008
	s_waitcnt vmcnt(8)
	ds_write_b32 v0, v26 offset:45056
	s_waitcnt vmcnt(7)
	ds_write_b32 v0, v27 offset:47104
	s_waitcnt vmcnt(6)
	ds_write_b32 v0, v28 offset:49152
	s_waitcnt vmcnt(5)
	ds_write_b32 v0, v29 offset:51200
	s_waitcnt vmcnt(4)
	ds_write_b32 v0, v30 offset:53248
	s_waitcnt vmcnt(3)
	ds_write_b32 v0, v31 offset:55296
	s_waitcnt vmcnt(2)
	ds_write_b32 v0, v32 offset:57344
	s_waitcnt vmcnt(1)
	ds_write_b32 v0, v33 offset:59392
	s_waitcnt vmcnt(0)
	ds_write_b32 v0, v34 offset:61440
